# nahead: NA unit head de-serialised (bias-table load overlaps the Q / first K,V tile loads; its full vmcnt(0) drain at every unit start removed)
# speedup vs baseline: 1.0016x; 1.0016x over previous
.LBB0_294:
	v_mov_b32_e32 v6, 0xff800000
	s_and_saveexec_b64 s[4:5], vcc
	s_cbranch_execz .LBB0_293
	s_load_dwordx2 s[28:29], s[10:11], 0x60
	v_ashrrev_i32_e32 v6, 5, v4
	v_mad_u64_u32 v[6:7], s[38:39], v6, 31, v[2:3]
	v_ashrrev_i32_e32 v7, 31, v6
	s_waitcnt lgkmcnt(0)
	v_lshl_add_u64 v[6:7], v[6:7], 2, s[28:29]
	global_load_dword v250, v[6:7], off
	v_mov_b32_e32 v251, v5
	v_mov_b32_e32 v6, 0xff800000
	s_branch .LBB0_293

.LBB0_298:
	v_and_b32_e32 v252, 31, v0
	v_xor_b32_e32 v252, 31, v252
	v_lshrrev_b32_e32 v253, 5, v0
	v_xor_b32_e32 v253, 15, v253
	v_mul_u32_u24_e32 v252, v252, v253
	v_cmp_ne_u32_e64 s[100:101], 0, v252
	s_and_b64 exec, exec, s[100:101]
	s_waitcnt vmcnt(6)
	v_mul_f32_e32 v250, 0x3fb8aa3b, v250
	ds_write_b32 v251, v250
	s_mov_b64 exec, -1
	s_and_b32 s4, s5, 0x3fffffc0
	s_lshl_b32 s4, s4, 2
	v_and_b32_e32 v163, 63, v7
	s_add_i32 s17, s4, 0
	v_mov_b32_e32 v35, 0
	s_cmp_lt_i32 s46, -4
	v_cmp_gt_u32_e64 s[4:5], 32, v163
	v_lshl_add_u32 v164, v6, 2, s17
	s_cbranch_scc1 .LBB0_347
	v_and_b32_e32 v8, 0x1fffff0, v96
	v_lshlrev_b32_e32 v9, 1, v96
	v_and_or_b32 v8, v9, 8, v8
	v_lshrrev_b32_e32 v8, 2, v8
	v_lshrrev_b32_e32 v5, 5, v5
	v_lshrrev_b32_e32 v9, 1, v96
	v_or_b32_e32 v5, v8, v5
	v_and_b32_e32 v8, 3, v96
	v_and_or_b32 v8, v9, 4, v8
	v_and_b32_e32 v9, 48, v2
	v_lshl_or_b32 v8, v8, 6, v9
	v_lshl_or_b32 v18, v5, 9, v8
	v_lshlrev_b32_e32 v8, 4, v163
	v_lshlrev_b32_e32 v5, 3, v163
	v_and_b32_e32 v8, 0xc0, v8
	v_lshlrev_b32_e32 v9, 1, v163
	v_and_or_b32 v8, v5, 24, v8
	v_and_b32_e32 v9, 32, v9
	v_and_b32_e32 v5, 0x100, v5
	v_or3_b32 v5, v8, v9, v5
	v_lshlrev_b32_e32 v8, 7, v96
	v_and_b32_e32 v7, 0x70, v7
	s_waitcnt vmcnt(9)
	v_lshl_add_u64 v[150:151], s[6:7], 0, v[2:3]
	v_lshl_add_u64 v[152:153], s[28:29], 0, v[2:3]
	v_bitop3_b32 v19, v2, v8, v7 bitop3:0xde
	v_lshlrev_b32_e32 v2, 7, v6
	v_lshlrev_b32_e32 v6, 3, v6
	v_and_b32_e32 v6, 0x70, v6
	v_or_b32_e32 v7, 32, v4
	s_waitcnt vmcnt(6)
	v_bitop3_b32 v156, v7, v2, v6 bitop3:0xde
	v_or_b32_e32 v7, 64, v4
	v_bitop3_b32 v157, v7, v2, v6 bitop3:0xde
	v_or_b32_e32 v7, 0x60, v4
	v_bitop3_b32 v155, v6, v2, v4 bitop3:0xde
	v_bitop3_b32 v158, v7, v2, v6 bitop3:0xde
	v_lshlrev_b32_e32 v2, 2, v162
	v_sub_u32_e32 v7, v2, v223
	v_or_b32_e32 v6, 32, v2
	v_add_u32_e32 v8, v2, v224
	v_cmp_gt_u32_e32 vcc, 16, v7
	v_or_b32_e32 v9, 33, v2
	v_or_b32_e32 v11, 34, v2
	v_cndmask_b32_e32 v7, 31, v8, vcc
	v_sub_u32_e32 v8, v6, v223
	v_cmp_gt_u32_e32 vcc, 16, v8
	v_or_b32_e32 v8, 1, v2
	v_add_u32_e32 v6, v6, v224
	v_sub_u32_e32 v10, v8, v223
	v_cndmask_b32_e32 v6, 31, v6, vcc
	v_add_u32_e32 v8, v8, v224
	v_cmp_gt_u32_e32 vcc, 16, v10
	v_sub_u32_e32 v10, v9, v223
	v_add_u32_e32 v9, v9, v224
	v_cndmask_b32_e32 v8, 31, v8, vcc
	v_cmp_gt_u32_e32 vcc, 16, v10
	v_or_b32_e32 v10, 2, v2
	v_sub_u32_e32 v12, v10, v223
	v_cndmask_b32_e32 v9, 31, v9, vcc
	v_add_u32_e32 v10, v10, v224
	v_cmp_gt_u32_e32 vcc, 16, v12
	v_sub_u32_e32 v12, v11, v223
	v_add_u32_e32 v11, v11, v224
	v_cndmask_b32_e32 v10, 31, v10, vcc
	v_cmp_gt_u32_e32 vcc, 16, v12
	v_or_b32_e32 v12, 3, v2
	v_or_b32_e32 v13, 35, v2
	v_sub_u32_e32 v14, v12, v223
	v_cndmask_b32_e32 v11, 31, v11, vcc
	v_add_u32_e32 v12, v12, v224
	v_cmp_gt_u32_e32 vcc, 16, v14
	v_sub_u32_e32 v14, v13, v223
	v_add_u32_e32 v13, v13, v224
	v_cndmask_b32_e32 v12, 31, v12, vcc
	v_cmp_gt_u32_e32 vcc, 16, v14
	v_or_b32_e32 v14, 8, v2
	v_or_b32_e32 v15, 40, v2
	v_sub_u32_e32 v16, v14, v223
	v_cndmask_b32_e32 v13, 31, v13, vcc
	v_add_u32_e32 v14, v14, v224
	v_cmp_gt_u32_e32 vcc, 16, v16
	v_sub_u32_e32 v16, v15, v223
	v_add_u32_e32 v15, v15, v224
	v_cndmask_b32_e32 v14, 31, v14, vcc
	v_cmp_gt_u32_e32 vcc, 16, v16
	v_or_b32_e32 v16, 9, v2
	v_or_b32_e32 v17, 41, v2
	v_sub_u32_e32 v20, v16, v223
	v_cndmask_b32_e32 v15, 31, v15, vcc
	v_add_u32_e32 v16, v16, v224
	v_cmp_gt_u32_e32 vcc, 16, v20
	v_sub_u32_e32 v20, v17, v223
	v_add_u32_e32 v17, v17, v224
	v_cndmask_b32_e32 v16, 31, v16, vcc
	v_cmp_gt_u32_e32 vcc, 16, v20
	v_or_b32_e32 v20, 10, v2
	v_or_b32_e32 v21, 42, v2
	v_sub_u32_e32 v22, v20, v223
	v_cndmask_b32_e32 v17, 31, v17, vcc
	v_add_u32_e32 v20, v20, v224
	v_cmp_gt_u32_e32 vcc, 16, v22
	v_sub_u32_e32 v22, v21, v223
	v_add_u32_e32 v21, v21, v224
	v_cndmask_b32_e32 v20, 31, v20, vcc
	v_cmp_gt_u32_e32 vcc, 16, v22
	v_or_b32_e32 v22, 11, v2
	v_or_b32_e32 v23, 43, v2
	v_sub_u32_e32 v24, v22, v223
	v_cndmask_b32_e32 v21, 31, v21, vcc
	v_add_u32_e32 v22, v22, v224
	v_cmp_gt_u32_e32 vcc, 16, v24
	v_sub_u32_e32 v24, v23, v223
	v_add_u32_e32 v23, v23, v224
	v_cndmask_b32_e32 v22, 31, v22, vcc
	v_cmp_gt_u32_e32 vcc, 16, v24
	v_or_b32_e32 v24, 16, v2
	v_sub_u32_e32 v26, v24, v223
	v_cndmask_b32_e32 v23, 31, v23, vcc
	v_or_b32_e32 v25, 48, v2
	v_add_u32_e32 v24, v24, v224
	v_cmp_gt_u32_e32 vcc, 16, v26
	v_add_u32_e32 v26, v25, v224
	v_or_b32_e32 v27, 49, v2
	v_cndmask_b32_e32 v24, 31, v24, vcc
	v_cmp_lt_u32_e32 vcc, v25, v225
	v_or_b32_e32 v29, 50, v2
	v_or_b32_e32 v31, 51, v2
	v_cndmask_b32_e32 v25, 31, v26, vcc
	v_or_b32_e32 v26, 17, v2
	v_sub_u32_e32 v28, v26, v223
	v_add_u32_e32 v26, v26, v224
	v_cmp_gt_u32_e32 vcc, 16, v28
	v_add_u32_e32 v28, v27, v224
	v_or_b32_e32 v33, 56, v2
	v_cndmask_b32_e32 v26, 31, v26, vcc
	v_cmp_lt_u32_e32 vcc, v27, v225
	v_or_b32_e32 v35, 57, v2
	s_add_i32 s38, s38, s55
	v_cndmask_b32_e32 v27, 31, v28, vcc
	v_or_b32_e32 v28, 18, v2
	v_sub_u32_e32 v30, v28, v223
	v_add_u32_e32 v28, v28, v224
	v_cmp_gt_u32_e32 vcc, 16, v30
	v_add_u32_e32 v30, v29, v224
	s_max_i32 s6, s38, 4
	v_cndmask_b32_e32 v28, 31, v28, vcc
	v_cmp_lt_u32_e32 vcc, v29, v225
	s_add_i32 s6, s6, -4
	s_min_u32 s6, s6, 0xf8
	v_cndmask_b32_e32 v29, 31, v30, vcc
	v_or_b32_e32 v30, 19, v2
	v_sub_u32_e32 v32, v30, v223
	v_add_u32_e32 v30, v30, v224
	v_cmp_gt_u32_e32 vcc, 16, v32
	v_add_u32_e32 v32, v31, v224
	v_or_b32_e32 v37, 58, v2
	v_cndmask_b32_e32 v30, 31, v30, vcc
	v_cmp_lt_u32_e32 vcc, v31, v225
	s_sub_i32 s65, s6, s12
	s_cmp_lg_u32 s59, -1
	v_cndmask_b32_e32 v31, 31, v32, vcc
	v_or_b32_e32 v32, 24, v2
	v_sub_u32_e32 v34, v32, v223
	v_add_u32_e32 v32, v32, v224
	v_cmp_gt_u32_e32 vcc, 16, v34
	v_add_u32_e32 v34, v33, v224
	s_cselect_b32 s6, s59, 0
	v_cndmask_b32_e32 v32, 31, v32, vcc
	v_cmp_lt_u32_e32 vcc, v33, v225
	s_and_b32 s7, s60, 63
	s_lshl_b32 s12, s7, 2
	v_cndmask_b32_e32 v33, 31, v34, vcc
	v_or_b32_e32 v34, 25, v2
	v_sub_u32_e32 v36, v34, v223
	v_add_u32_e32 v34, v34, v224
	v_cmp_gt_u32_e32 vcc, 16, v36
	v_add_u32_e32 v36, v35, v224
	s_max_i32 s12, s12, 4
	v_cndmask_b32_e32 v34, 31, v34, vcc
	v_cmp_lt_u32_e32 vcc, v35, v225
	v_add_u32_e32 v154, s6, v5
	s_lshl_b32 s12, s12, 7
	v_cndmask_b32_e32 v35, 31, v36, vcc
	v_or_b32_e32 v36, 26, v2
	v_sub_u32_e32 v38, v36, v223
	v_add_u32_e32 v36, v36, v224
	v_cmp_gt_u32_e32 vcc, 16, v38
	v_add_u32_e32 v38, v37, v224
	s_lshl_b32 s7, s7, 9
	v_cndmask_b32_e32 v36, 31, v36, vcc
	v_cmp_lt_u32_e32 vcc, v37, v225
	s_addk_i32 s6, 0x2000
	v_lshlrev_b32_e32 v184, 2, v17
	v_cndmask_b32_e32 v37, 31, v38, vcc
	v_or_b32_e32 v38, 27, v2
	v_sub_u32_e32 v39, v38, v223
	v_or_b32_e32 v2, 59, v2
	v_add_u32_e32 v38, v38, v224
	v_cmp_gt_u32_e32 vcc, 16, v39
	v_add_u32_e32 v39, v2, v224
	v_lshlrev_b32_e32 v185, 2, v16
	v_cndmask_b32_e32 v38, 31, v38, vcc
	v_cmp_lt_u32_e32 vcc, v2, v225
	v_mov_b32_e32 v16, v3
	v_mov_b32_e32 v17, v3
	v_cndmask_b32_e32 v2, 31, v39, vcc
	s_sub_i32 s7, s12, s7
	v_add_u32_e32 v159, s17, v4
	v_add_u32_e32 v160, s6, v5
	v_lshlrev_b32_e32 v161, 2, v2
	v_lshlrev_b32_e32 v165, 2, v38
	v_lshlrev_b32_e32 v166, 2, v37
	v_lshlrev_b32_e32 v167, 2, v36
	v_lshlrev_b32_e32 v186, 2, v15
	v_lshlrev_b32_e32 v187, 2, v14
	v_lshlrev_b32_e32 v188, 2, v13
	v_lshlrev_b32_e32 v189, 2, v12
	v_lshlrev_b32_e32 v190, 2, v11
	v_lshlrev_b32_e32 v191, 2, v10
	v_lshlrev_b32_e32 v192, 2, v9
	v_lshlrev_b32_e32 v193, 2, v8
	v_lshlrev_b32_e32 v198, 2, v6
	v_lshlrev_b32_e32 v199, 2, v7
	v_mov_b32_e32 v2, v3
	v_mov_b32_e32 v4, v3
	v_mov_b32_e32 v5, v3
	v_mov_b32_e32 v6, v3
	v_mov_b32_e32 v7, v3
	v_mov_b32_e32 v8, v3
	v_mov_b32_e32 v9, v3
	v_mov_b32_e32 v10, v3
	v_mov_b32_e32 v11, v3
	v_mov_b32_e32 v12, v3
	v_mov_b32_e32 v13, v3
	v_mov_b32_e32 v14, v3
	v_mov_b32_e32 v15, v3
	v_mov_b32_e32 v203, 0
	v_mov_b64_e32 v[50:51], v[16:17]
	s_movk_i32 s66, 0xc0
	s_mov_b32 s72, 0
	s_add_i32 s67, s46, 5
	s_add_i32 s68, s3, s7
	s_add_i32 s69, s65, 8
	s_add_i32 s70, s65, 7
	v_lshlrev_b32_e32 v168, 2, v35
	v_lshlrev_b32_e32 v169, 2, v34
	v_lshlrev_b32_e32 v170, 2, v33
	v_lshlrev_b32_e32 v171, 2, v32
	v_lshlrev_b32_e32 v172, 2, v31
	v_lshlrev_b32_e32 v173, 2, v30
	v_lshlrev_b32_e32 v174, 2, v29
	v_lshlrev_b32_e32 v175, 2, v28
	v_lshlrev_b32_e32 v176, 2, v27
	v_lshlrev_b32_e32 v177, 2, v26
	v_lshlrev_b32_e32 v178, 2, v25
	v_lshlrev_b32_e32 v179, 2, v24
	v_lshlrev_b32_e32 v180, 2, v23
	v_lshlrev_b32_e32 v181, 2, v22
	v_lshlrev_b32_e32 v182, 2, v21
	v_lshlrev_b32_e32 v183, 2, v20
	s_mov_b64 s[6:7], -1
	v_add_u32_e32 v200, 0, v19
	v_add_u32_e32 v201, 0, v18
	v_mov_b64_e32 v[48:49], v[14:15]
	v_mov_b64_e32 v[46:47], v[12:13]
	v_mov_b64_e32 v[44:45], v[10:11]
	v_mov_b64_e32 v[42:43], v[8:9]
	v_mov_b64_e32 v[40:41], v[6:7]
	v_mov_b64_e32 v[38:39], v[4:5]
	v_mov_b64_e32 v[36:37], v[2:3]
	v_mov_b32_e32 v202, 0
	v_mov_b32_e32 v4, 0
	v_mov_b32_e32 v5, v203
	v_mov_b32_e32 v6, v203
	v_mov_b32_e32 v7, v203
	v_mov_b32_e32 v8, v203
	v_mov_b32_e32 v9, v203
	v_mov_b32_e32 v10, v203
	v_mov_b32_e32 v11, v203
	v_mov_b32_e32 v12, v203
	v_mov_b32_e32 v13, v203
	v_mov_b32_e32 v14, v203
	v_mov_b32_e32 v15, v203
	v_mov_b32_e32 v16, v203
	v_mov_b32_e32 v17, v203
	v_mov_b32_e32 v18, v203
	v_mov_b32_e32 v19, v203
	v_mov_b32_e32 v20, v203
	v_mov_b32_e32 v21, v203
	v_mov_b32_e32 v22, v203
	v_mov_b32_e32 v23, v203
	v_mov_b32_e32 v24, v203
	v_mov_b32_e32 v25, v203
	v_mov_b32_e32 v26, v203
	v_mov_b32_e32 v27, v203
	v_mov_b32_e32 v28, v203
	v_mov_b32_e32 v29, v203
	v_mov_b32_e32 v30, v203
	v_mov_b32_e32 v31, v203
	v_mov_b32_e32 v32, v203
	v_mov_b32_e32 v33, v203
	v_mov_b32_e32 v34, v203
	v_mov_b32_e32 v35, v203
